# v22 + every workgroup starts an L2 write-back when it arrives at the grid barrier (leader release finds little left)
# baseline (speedup 1.0000x reference)
; __device__ __forceinline__ void xcd_barrier(const XcdBarrier& b) {
;     asm volatile("s_waitcnt vmcnt(0)" ::: "memory");
;     __syncthreads();
;     if (threadIdx.x == 0) {
;         unsigned* bar = b.bar; unsigned bx = b.x;
;         asm volatile("" : "+s"(bar), "+s"(bx));
;         __builtin_amdgcn_s_waitcnt(0);
;         unsigned nloc = b.st[0], nx = b.st[1];
;         if (nloc == 0u) { xcd_barrier_complete(bar, bx, nloc, nx); b.st[0] = nloc; b.st[1] = nx; }
.LBB0_57:
	s_waitcnt vmcnt(0)
	s_barrier
	s_mov_b64 s[0:1], exec
	v_readlane_b32 s2, v252, 3
	v_readlane_b32 s3, v252, 4
	s_and_b64 s[2:3], s[0:1], s[2:3]
	s_mov_b64 exec, s[2:3]
	s_cbranch_execz .LBB0_101
	buffer_wbl2 sc1
	v_readlane_b32 s38, v252, 0
	s_add_i32 s3, 0, 0x21c20
	v_readlane_b32 s2, v252, 2
	v_readlane_b32 s39, v252, 1
	s_waitcnt vmcnt(34)
	v_mov_b32_e32 v1, s3
	s_waitcnt vmcnt(0) expcnt(0) lgkmcnt(0)
	ds_read_b32 v4, v1
	s_add_i32 s3, 0, 0x21c24
	v_mov_b32_e32 v1, s3
	ds_read_b32 v2, v1
	s_waitcnt lgkmcnt(1)
	v_cmp_ne_u32_e32 vcc, 0, v4
	s_cbranch_vccnz .LBB0_72
	v_readlane_b32 s6, v252, 5
	v_readlane_b32 s7, v252, 6
	s_load_dwordx2 s[4:5], s[6:7], 0x4
	s_add_u32 s6, s38, 0x1000
	s_addc_u32 s7, s39, 0
	s_add_u32 s8, s38, 0x1100
	s_addc_u32 s9, s39, 0
	s_add_u32 s10, s38, 0x1200
	s_addc_u32 s11, s39, 0
	s_add_u32 s12, s38, 0x1300
	s_waitcnt lgkmcnt(0)
	s_mul_i32 s3, s4, s77
	s_addc_u32 s13, s39, 0
	s_mul_i32 s3, s3, s5
	s_mov_b32 s22, 1
	s_mov_b64 s[4:5], 0
	v_mov_b64_e32 v[2:3], s[38:39]
	v_mov_b64_e32 v[4:5], s[6:7]
	v_mov_b64_e32 v[6:7], s[8:9]
	v_mov_b64_e32 v[8:9], s[10:11]
	v_mov_b64_e32 v[10:11], s[12:13]
	s_branch .LBB0_62

; __device__ __forceinline__ void xcd_barrier(const XcdBarrier& b) {
;     asm volatile("s_waitcnt vmcnt(0)" ::: "memory");
;     __syncthreads();
;     if (threadIdx.x == 0) {
;         unsigned* bar = b.bar; unsigned bx = b.x;
;         asm volatile("" : "+s"(bar), "+s"(bx));
;         __builtin_amdgcn_s_waitcnt(0);
;         unsigned nloc = b.st[0], nx = b.st[1];
;         if (nloc == 0u) { xcd_barrier_complete(bar, bx, nloc, nx); b.st[0] = nloc; b.st[1] = nx; }
.LBB0_156:
	s_or_b64 exec, exec, s[12:13]
	s_waitcnt lgkmcnt(0)
	s_barrier
	s_waitcnt vmcnt(0)
	s_barrier
	s_mov_b64 s[38:39], exec
	v_readlane_b32 s4, v252, 3
	v_readlane_b32 s5, v252, 4
	s_and_b64 s[4:5], s[38:39], s[4:5]
	s_mov_b64 exec, s[4:5]
	s_cbranch_execz .LBB0_200
	buffer_wbl2 sc1
	v_readlane_b32 s40, v252, 0
	v_readlane_b32 s4, v253, 50
	v_readlane_b32 s41, v252, 1
	v_readlane_b32 s2, v252, 2
	v_mov_b32_e32 v1, s4
	s_waitcnt vmcnt(0) expcnt(0) lgkmcnt(0)
	ds_read_b32 v4, v1
	v_readlane_b32 s4, v253, 51
	s_waitcnt lgkmcnt(0)
	v_cmp_ne_u32_e32 vcc, 0, v4
	v_mov_b32_e32 v1, s4
	ds_read_b32 v2, v1
	s_cbranch_vccnz .LBB0_171
	v_readlane_b32 s4, v252, 5
	v_readlane_b32 s5, v252, 6
	s_load_dwordx2 s[8:9], s[4:5], 0x4
	s_add_u32 s4, s40, 0x1000
	s_addc_u32 s5, s41, 0
	s_add_u32 s6, s40, 0x1100
	s_addc_u32 s7, s41, 0
	s_waitcnt lgkmcnt(0)
	s_mul_i32 s30, s8, s77
	s_add_u32 s8, s40, 0x1200
	s_mul_i32 s30, s30, s9
	s_addc_u32 s9, s41, 0
	s_add_u32 s10, s40, 0x1300
	s_addc_u32 s11, s41, 0
	s_mov_b32 s31, 1
	s_mov_b64 s[12:13], 0
	s_branch .LBB0_161

; __device__ __forceinline__ void xcd_barrier(const XcdBarrier& b) {
;     asm volatile("s_waitcnt vmcnt(0)" ::: "memory");
;     __syncthreads();
;     if (threadIdx.x == 0) {
;         unsigned* bar = b.bar; unsigned bx = b.x;
;         asm volatile("" : "+s"(bar), "+s"(bx));
;         __builtin_amdgcn_s_waitcnt(0);
;         unsigned nloc = b.st[0], nx = b.st[1];
;         if (nloc == 0u) { xcd_barrier_complete(bar, bx, nloc, nx); b.st[0] = nloc; b.st[1] = nx; }
.LBB0_346:
	s_waitcnt vmcnt(0)
	s_waitcnt vmcnt(0)
	s_barrier
	s_mov_b64 s[38:39], exec
	v_readlane_b32 s4, v252, 3
	v_readlane_b32 s5, v252, 4
	s_and_b64 s[4:5], s[38:39], s[4:5]
	s_mov_b64 exec, s[4:5]
	s_cbranch_execz .LBB0_390
	buffer_wbl2 sc1
	v_readlane_b32 s40, v252, 0
	v_readlane_b32 s4, v253, 50
	v_readlane_b32 s41, v252, 1
	v_readlane_b32 s2, v252, 2
	v_mov_b32_e32 v1, s4
	s_waitcnt vmcnt(0) expcnt(0) lgkmcnt(0)
	ds_read_b32 v4, v1
	v_readlane_b32 s4, v253, 51
	s_waitcnt lgkmcnt(0)
	v_cmp_ne_u32_e32 vcc, 0, v4
	v_mov_b32_e32 v1, s4
	ds_read_b32 v2, v1
	s_cbranch_vccnz .LBB0_361
	v_readlane_b32 s4, v252, 5
	v_readlane_b32 s5, v252, 6
	s_load_dwordx2 s[8:9], s[4:5], 0x4
	s_add_u32 s4, s40, 0x1000
	s_addc_u32 s5, s41, 0
	s_add_u32 s6, s40, 0x1100
	s_addc_u32 s7, s41, 0
	s_waitcnt lgkmcnt(0)
	s_mul_i32 s30, s8, s77
	s_add_u32 s8, s40, 0x1200
	s_mul_i32 s30, s30, s9
	s_addc_u32 s9, s41, 0
	s_add_u32 s10, s40, 0x1300
	s_addc_u32 s11, s41, 0
	s_mov_b32 s31, 1
	s_mov_b64 s[12:13], 0
	s_branch .LBB0_351

; __device__ __forceinline__ void xcd_barrier(const XcdBarrier& b) {
;     asm volatile("s_waitcnt vmcnt(0)" ::: "memory");
;     __syncthreads();
;     if (threadIdx.x == 0) {
;         unsigned* bar = b.bar; unsigned bx = b.x;
;         asm volatile("" : "+s"(bar), "+s"(bx));
;         __builtin_amdgcn_s_waitcnt(0);
;         unsigned nloc = b.st[0], nx = b.st[1];
;         if (nloc == 0u) { xcd_barrier_complete(bar, bx, nloc, nx); b.st[0] = nloc; b.st[1] = nx; }
.LBB0_601:
	s_waitcnt vmcnt(0) lgkmcnt(0)
	s_barrier
	s_waitcnt vmcnt(0)
	s_waitcnt lgkmcnt(0)
	s_barrier
	s_mov_b64 s[38:39], exec
	v_readlane_b32 s4, v252, 3
	v_readlane_b32 s5, v252, 4
	s_and_b64 s[4:5], s[38:39], s[4:5]
	s_mov_b64 exec, s[4:5]
	s_cbranch_execz .LBB0_645
	buffer_wbl2 sc1
	v_readlane_b32 s40, v252, 0
	v_readlane_b32 s4, v253, 50
	v_readlane_b32 s41, v252, 1
	v_readlane_b32 s2, v252, 2
	v_mov_b32_e32 v1, s4
	s_waitcnt vmcnt(0) expcnt(0) lgkmcnt(0)
	ds_read_b32 v4, v1
	v_readlane_b32 s4, v253, 51
	s_waitcnt lgkmcnt(0)
	v_cmp_ne_u32_e32 vcc, 0, v4
	v_mov_b32_e32 v1, s4
	ds_read_b32 v2, v1
	s_cbranch_vccnz .LBB0_616
	v_readlane_b32 s4, v252, 5
	v_readlane_b32 s5, v252, 6
	s_load_dwordx2 s[8:9], s[4:5], 0x4
	s_add_u32 s4, s40, 0x1000
	s_addc_u32 s5, s41, 0
	s_add_u32 s6, s40, 0x1100
	s_addc_u32 s7, s41, 0
	s_waitcnt lgkmcnt(0)
	s_mul_i32 s30, s8, s77
	s_add_u32 s8, s40, 0x1200
	s_mul_i32 s30, s30, s9
	s_addc_u32 s9, s41, 0
	s_add_u32 s10, s40, 0x1300
	s_addc_u32 s11, s41, 0
	s_mov_b32 s31, 1
	s_mov_b64 s[12:13], 0
	s_branch .LBB0_606

; __device__ __forceinline__ void xcd_barrier(const XcdBarrier& b) {
;     asm volatile("s_waitcnt vmcnt(0)" ::: "memory");
;     __syncthreads();
;     if (threadIdx.x == 0) {
;         unsigned* bar = b.bar; unsigned bx = b.x;
;         asm volatile("" : "+s"(bar), "+s"(bx));
;         __builtin_amdgcn_s_waitcnt(0);
;         unsigned nloc = b.st[0], nx = b.st[1];
;         if (nloc == 0u) { xcd_barrier_complete(bar, bx, nloc, nx); b.st[0] = nloc; b.st[1] = nx; }
.LBB0_660:
	s_or_b64 exec, exec, s[10:11]
	s_waitcnt vmcnt(0)
	s_barrier
	s_mov_b64 s[38:39], exec
	v_readlane_b32 s4, v252, 3
	v_readlane_b32 s5, v252, 4
	s_and_b64 s[4:5], s[38:39], s[4:5]
	s_mov_b64 exec, s[4:5]
	s_cbranch_execz .LBB0_704
	buffer_wbl2 sc1
	v_readlane_b32 s40, v252, 0
	v_readlane_b32 s4, v253, 50
	v_readlane_b32 s41, v252, 1
	v_readlane_b32 s2, v252, 2
	v_mov_b32_e32 v1, s4
	s_waitcnt vmcnt(0) expcnt(0) lgkmcnt(0)
	ds_read_b32 v4, v1
	v_readlane_b32 s4, v253, 51
	s_waitcnt lgkmcnt(0)
	v_cmp_ne_u32_e32 vcc, 0, v4
	v_mov_b32_e32 v1, s4
	ds_read_b32 v2, v1
	s_cbranch_vccnz .LBB0_675
	v_readlane_b32 s4, v252, 5
	v_readlane_b32 s5, v252, 6
	s_load_dwordx2 s[8:9], s[4:5], 0x4
	s_add_u32 s4, s40, 0x1000
	s_addc_u32 s5, s41, 0
	s_add_u32 s6, s40, 0x1100
	s_addc_u32 s7, s41, 0
	s_waitcnt lgkmcnt(0)
	s_mul_i32 s30, s8, s77
	s_add_u32 s8, s40, 0x1200
	s_mul_i32 s30, s30, s9
	s_addc_u32 s9, s41, 0
	s_add_u32 s10, s40, 0x1300
	s_addc_u32 s11, s41, 0
	s_mov_b32 s31, 1
	s_mov_b64 s[12:13], 0
	s_branch .LBB0_665

; __device__ __forceinline__ void xcd_barrier(const XcdBarrier& b) {
;     asm volatile("s_waitcnt vmcnt(0)" ::: "memory");
;     __syncthreads();
;     if (threadIdx.x == 0) {
;         unsigned* bar = b.bar; unsigned bx = b.x;
;         asm volatile("" : "+s"(bar), "+s"(bx));
;         __builtin_amdgcn_s_waitcnt(0);
;         unsigned nloc = b.st[0], nx = b.st[1];
;         if (nloc == 0u) { xcd_barrier_complete(bar, bx, nloc, nx); b.st[0] = nloc; b.st[1] = nx; }
.LBB0_728:
	s_waitcnt vmcnt(0)
	s_waitcnt vmcnt(0)
	s_barrier
	s_mov_b64 s[36:37], exec
	v_readlane_b32 s4, v252, 3
	v_readlane_b32 s5, v252, 4
	s_and_b64 s[4:5], s[36:37], s[4:5]
	s_mov_b64 exec, s[4:5]
	s_cbranch_execz .LBB0_772
	buffer_wbl2 sc1
	v_readlane_b32 s38, v252, 0
	v_readlane_b32 s4, v253, 50
	v_readlane_b32 s39, v252, 1
	v_readlane_b32 s2, v252, 2
	v_mov_b32_e32 v1, s4
	s_waitcnt vmcnt(0) expcnt(0) lgkmcnt(0)
	ds_read_b32 v4, v1
	v_readlane_b32 s4, v253, 51
	s_waitcnt lgkmcnt(0)
	v_cmp_ne_u32_e32 vcc, 0, v4
	v_mov_b32_e32 v1, s4
	ds_read_b32 v2, v1
	s_cbranch_vccnz .LBB0_743
	v_readlane_b32 s4, v252, 5
	v_readlane_b32 s5, v252, 6
	s_load_dwordx2 s[8:9], s[4:5], 0x4
	s_add_u32 s4, s38, 0x1000
	s_addc_u32 s5, s39, 0
	s_add_u32 s6, s38, 0x1100
	s_addc_u32 s7, s39, 0
	s_waitcnt lgkmcnt(0)
	s_mul_i32 s30, s8, s77
	s_add_u32 s8, s38, 0x1200
	s_mul_i32 s30, s30, s9
	s_addc_u32 s9, s39, 0
	s_add_u32 s10, s38, 0x1300
	s_addc_u32 s11, s39, 0
	s_mov_b32 s31, 1
	s_mov_b64 s[12:13], 0
	s_branch .LBB0_733

; __device__ __forceinline__ void xcd_barrier(const XcdBarrier& b) {
;     asm volatile("s_waitcnt vmcnt(0)" ::: "memory");
;     __syncthreads();
;     if (threadIdx.x == 0) {
;         unsigned* bar = b.bar; unsigned bx = b.x;
;         asm volatile("" : "+s"(bar), "+s"(bx));
;         __builtin_amdgcn_s_waitcnt(0);
;         unsigned nloc = b.st[0], nx = b.st[1];
;         if (nloc == 0u) { xcd_barrier_complete(bar, bx, nloc, nx); b.st[0] = nloc; b.st[1] = nx; }
.LBB0_854:
	s_waitcnt vmcnt(0)
	s_barrier
	s_mov_b64 s[36:37], exec
	v_readlane_b32 s4, v252, 3
	v_readlane_b32 s5, v252, 4
	s_and_b64 s[4:5], s[36:37], s[4:5]
	s_mov_b64 exec, s[4:5]
	s_cbranch_execz .LBB0_898
	buffer_wbl2 sc1
	v_readlane_b32 s38, v252, 0
	v_readlane_b32 s4, v253, 50
	v_readlane_b32 s2, v252, 2
	v_readlane_b32 s39, v252, 1
	v_mov_b32_e32 v1, s4
	s_waitcnt vmcnt(0) expcnt(0) lgkmcnt(0)
	ds_read_b32 v4, v1
	v_readlane_b32 s4, v253, 51
	s_waitcnt lgkmcnt(0)
	v_cmp_ne_u32_e32 vcc, 0, v4
	v_mov_b32_e32 v1, s4
	ds_read_b32 v2, v1
	s_cbranch_vccnz .LBB0_869
	v_readlane_b32 s4, v252, 5
	v_readlane_b32 s5, v252, 6
	s_load_dwordx2 s[8:9], s[4:5], 0x4
	s_add_u32 s4, s38, 0x1000
	s_addc_u32 s5, s39, 0
	s_add_u32 s6, s38, 0x1100
	s_addc_u32 s7, s39, 0
	s_waitcnt lgkmcnt(0)
	s_mul_i32 s30, s8, s77
	s_add_u32 s8, s38, 0x1200
	s_mul_i32 s30, s30, s9
	s_addc_u32 s9, s39, 0
	s_add_u32 s10, s38, 0x1300
	s_addc_u32 s11, s39, 0
	s_mov_b32 s31, 1
	s_mov_b64 s[12:13], 0
	s_branch .LBB0_859

; __device__ __forceinline__ void xcd_barrier(const XcdBarrier& b) {
;     asm volatile("s_waitcnt vmcnt(0)" ::: "memory");
;     __syncthreads();
;     if (threadIdx.x == 0) {
;         unsigned* bar = b.bar; unsigned bx = b.x;
;         asm volatile("" : "+s"(bar), "+s"(bx));
;         __builtin_amdgcn_s_waitcnt(0);
;         unsigned nloc = b.st[0], nx = b.st[1];
;         if (nloc == 0u) { xcd_barrier_complete(bar, bx, nloc, nx); b.st[0] = nloc; b.st[1] = nx; }
.LBB0_1112:
	v_readlane_b32 vcc_lo, v254, 62
	s_nop 1
	s_cmp_eq_u32 vcc_lo, 1
	s_cbranch_scc1 .Ltail_signal
	s_waitcnt vmcnt(0)
	s_waitcnt vmcnt(0)
	s_barrier
	s_mov_b64 s[36:37], exec
	v_readlane_b32 s4, v252, 3
	v_readlane_b32 s5, v252, 4
	s_and_b64 s[4:5], s[36:37], s[4:5]
	s_mov_b64 exec, s[4:5]
	s_cbranch_execz .LBB0_1156
	buffer_wbl2 sc1
	v_readlane_b32 s38, v252, 0
	v_readlane_b32 s4, v253, 50
	v_readlane_b32 s39, v252, 1
	v_readlane_b32 s2, v252, 2
	v_mov_b32_e32 v1, s4
	s_waitcnt vmcnt(0) expcnt(0) lgkmcnt(0)
	ds_read_b32 v4, v1
	v_readlane_b32 s4, v253, 51
	s_waitcnt lgkmcnt(0)
	v_cmp_ne_u32_e32 vcc, 0, v4
	v_mov_b32_e32 v1, s4
	ds_read_b32 v2, v1
	s_cbranch_vccnz .LBB0_1127
	v_readlane_b32 s4, v252, 5
	v_readlane_b32 s5, v252, 6
	s_load_dwordx2 s[8:9], s[4:5], 0x4
	s_add_u32 s4, s38, 0x1000
	s_addc_u32 s5, s39, 0
	s_add_u32 s6, s38, 0x1100
	s_addc_u32 s7, s39, 0
	s_waitcnt lgkmcnt(0)
	s_mul_i32 s30, s8, s77
	s_add_u32 s8, s38, 0x1200
	s_mul_i32 s30, s30, s9
	s_addc_u32 s9, s39, 0
	s_add_u32 s10, s38, 0x1300
	s_addc_u32 s11, s39, 0
	s_mov_b32 s31, 1
	s_mov_b64 s[12:13], 0
	s_branch .LBB0_1117
